# speedup vs baseline: 1.0189x; 1.0024x over previous
_Z7k0_prepPKfS0_S0_S0_S0_S0_S0_S0_S0_S0_S0_S0_S0_Pf:
	s_movk_i32 s3, 0xffb3
	s_cmp_lt_u32 s2, 0x1cd
	s_cselect_b32 s3, 31, s3
	s_cmp_lt_u32 s2, 0x180
	s_cselect_b32 s3, 0, s3
	s_add_i32 s2, s2, s3
	s_load_dwordx2 s[8:9], s[0:1], 0x68
	s_cmpk_gt_i32 s2, 0x17f
	s_mov_b64 s[4:5], -1
	s_cbranch_scc0 .LBB0_71
	s_cmpk_lt_u32 s2, 0x19f
	s_cbranch_scc0 .LBB0_42
	s_load_dwordx2 s[4:5], s[0:1], 0x30
	s_cmpk_lg_i32 s2, 0x19e
	s_mov_b64 s[6:7], -1
	s_cbranch_scc0 .LBB0_34
	s_load_dwordx2 s[6:7], s[0:1], 0x20
	v_lshl_or_b32 v1, s2, 8, v0
	v_add_u32_e32 v2, 0xfffe8000, v1
	s_movk_i32 s3, 0x1a00
	v_cmp_gt_u32_e32 vcc, s3, v2
	s_and_saveexec_b64 s[10:11], vcc
	s_xor_b64 s[10:11], exec, s[10:11]
	s_cbranch_execz .LBB0_29
	v_lshrrev_b32_e32 v3, 6, v2
	s_movk_i32 s3, 0x1ff
	v_add_u32_e32 v4, 4, v3
	v_cmp_lt_u32_e32 vcc, s3, v2
	v_and_b32_e32 v1, 63, v0
	v_and_b32_e32 v7, 15, v0
	v_cndmask_b32_e32 v5, v3, v4, vcc
	v_subrev_u32_e32 v2, 36, v5
	v_bfe_u32 v6, v0, 4, 2
	v_cmp_lt_u32_e32 vcc, 7, v2
	s_and_saveexec_b64 s[12:13], vcc
	s_xor_b64 s[12:13], exec, s[12:13]
	s_cbranch_execz .LBB0_26
	v_cmp_lt_u32_e32 vcc, 7, v5
	s_and_saveexec_b64 s[14:15], vcc
	s_xor_b64 s[14:15], exec, s[14:15]
	s_cbranch_execz .LBB0_23
	v_cmp_lt_u32_e32 vcc, 19, v5
	s_and_saveexec_b64 s[16:17], vcc
	s_xor_b64 s[16:17], exec, s[16:17]
	s_cbranch_execz .LBB0_20
	v_cmp_lt_u32_e32 vcc, 27, v5
	s_and_saveexec_b64 s[18:19], vcc
	s_xor_b64 s[18:19], exec, s[18:19]
	s_cbranch_execz .LBB0_17
	v_cmp_lt_u32_e32 vcc, 35, v5
	s_and_saveexec_b64 s[20:21], vcc
	s_xor_b64 s[20:21], exec, s[20:21]
	s_cbranch_execz .LBB0_14
	s_load_dwordx2 s[22:23], s[0:1], 0x60
	s_movk_i32 s3, 0x4b
	v_cmp_lt_u32_e32 vcc, s3, v5
	s_and_saveexec_b64 s[24:25], vcc
	s_xor_b64 s[24:25], exec, s[24:25]
	v_add_u32_e32 v2, 0xffffffb4, v5
	v_lshrrev_b32_e32 v9, 3, v2
	v_and_b32_e32 v8, 7, v2
	s_or_saveexec_b64 s[24:25], s[24:25]
	v_mov_b32_e32 v10, 0x100
	s_waitcnt lgkmcnt(0)
	v_mov_b64_e32 v[2:3], s[22:23]
	s_xor_b64 exec, exec, s[24:25]
	s_cbranch_execz .LBB0_13
	s_load_dwordx2 s[22:23], s[0:1], 0x58
	v_subrev_u32_e32 v2, 44, v5
	v_ashrrev_i32_e32 v9, 1, v2
	v_and_b32_e32 v8, 1, v5
	v_mov_b32_e32 v10, 64
	s_waitcnt lgkmcnt(0)
	v_mov_b64_e32 v[2:3], s[22:23]
